# NA output: four 4-byte stores per lane merged into one 16-byte store via permlane16/32 swap transposes; unreachable padding keeps the later hot loops at their previous instruction-fetch alignment
# speedup vs baseline: 1.0299x; 1.0009x over previous
.LBB0_614:
	s_or_b64 exec, exec, s[30:31]
	s_mov_b32 s4, 0xff800000
	v_max3_f32 v82, v101, s4, v100
	v_max3_f32 v82, v82, v103, v102
	v_max3_f32 v82, v82, v145, v144
	v_max3_f32 v82, v82, v146, v140
	v_max3_f32 v82, v82, v142, v141
	v_max3_f32 v82, v82, v137, v136
	v_max3_f32 v82, v82, v139, v138
	v_max3_f32 v82, v82, v133, v132
	v_max3_f32 v82, v82, v135, v134
	v_max3_f32 v82, v82, v129, v128
	v_max3_f32 v82, v82, v131, v130
	v_max3_f32 v82, v82, v125, v124
	v_max3_f32 v82, v82, v127, v126
	v_max3_f32 v82, v82, v121, v120
	v_max3_f32 v82, v82, v123, v122
	v_max3_f32 v82, v82, v117, v116
	v_max3_f32 v82, v82, v119, v118
	v_max3_f32 v82, v82, v147, v112
	v_max3_f32 v82, v82, v192, v114
	v_max3_f32 v82, v82, v193, v109
	v_max3_f32 v82, v82, v194, v111
	v_max3_f32 v82, v82, v105, v104
	v_max3_f32 v82, v82, v196, v195
	v_max3_f32 v82, v82, v97, v96
	v_max3_f32 v82, v82, v99, v98
	v_max3_f32 v82, v82, v93, v92
	v_max3_f32 v82, v82, v95, v94
	v_max3_f32 v82, v82, v89, v88
	v_max3_f32 v82, v82, v91, v90
	v_max3_f32 v82, v82, v198, v197
	v_max3_f32 v82, v82, v202, v199
	v_max3_f32 v82, v82, v81, v80
	v_mov_b32 v83, v82
	ds_bpermute_b32 v83, v170, v83
	s_mov_b32 s34, s60
	s_waitcnt lgkmcnt(0)
	v_max_f32_e32 v83, v83, v83
	v_max_f32_e32 v82, v82, v83
	v_mov_b32 v83, v82
	ds_bpermute_b32 v83, v171, v83
	s_waitcnt lgkmcnt(0)
	v_max_f32_e32 v83, v83, v83
	v_max_f32_e32 v82, v82, v83
	v_sub_f32_e32 v83, v101, v82
	v_sub_f32_e32 v84, v100, v82
	v_exp_f32_e32 v83, v83
	v_sub_f32_e32 v85, v103, v82
	v_exp_f32_e32 v143, v84
	v_sub_f32_e32 v86, v102, v82
	v_sub_f32_e32 v100, v144, v82
	v_exp_f32_e32 v144, v85
	v_sub_f32_e32 v87, v145, v82
	v_exp_f32_e32 v145, v86
	v_sub_f32_e32 v101, v146, v82
	v_exp_f32_e32 v146, v87
	v_add_f32_e32 v84, 0, v83
	v_exp_f32_e32 v191, v100
	v_add_f32_e32 v84, v143, v84
	v_add_f32_e32 v84, v144, v84
	v_exp_f32_e32 v203, v101
	v_sub_f32_e32 v85, v140, v82
	v_add_f32_e32 v84, v145, v84
	v_exp_f32_e32 v140, v85
	v_sub_f32_e32 v85, v142, v82
	v_add_f32_e32 v84, v146, v84
	v_exp_f32_e32 v204, v85
	v_sub_f32_e32 v85, v141, v82
	v_add_f32_e32 v84, v191, v84
	v_exp_f32_e32 v205, v85
	v_sub_f32_e32 v85, v137, v82
	v_add_f32_e32 v84, v203, v84
	v_exp_f32_e32 v206, v85
	v_sub_f32_e32 v85, v136, v82
	v_add_f32_e32 v84, v140, v84
	v_exp_f32_e32 v207, v85
	v_sub_f32_e32 v85, v139, v82
	v_add_f32_e32 v84, v204, v84
	v_exp_f32_e32 v208, v85
	v_sub_f32_e32 v85, v138, v82
	v_add_f32_e32 v84, v205, v84
	v_exp_f32_e32 v209, v85
	v_sub_f32_e32 v85, v133, v82
	v_add_f32_e32 v84, v206, v84
	v_exp_f32_e32 v210, v85
	v_sub_f32_e32 v85, v132, v82
	v_add_f32_e32 v84, v207, v84
	v_exp_f32_e32 v211, v85
	v_sub_f32_e32 v85, v135, v82
	v_add_f32_e32 v84, v208, v84
	v_exp_f32_e32 v132, v85
	v_sub_f32_e32 v85, v134, v82
	v_add_f32_e32 v84, v209, v84
	v_exp_f32_e32 v133, v85
	v_sub_f32_e32 v85, v129, v82
	v_add_f32_e32 v84, v210, v84
	v_exp_f32_e32 v129, v85
	v_sub_f32_e32 v85, v128, v82
	v_add_f32_e32 v84, v211, v84
	v_exp_f32_e32 v128, v85
	v_sub_f32_e32 v85, v131, v82
	v_add_f32_e32 v84, v132, v84
	v_exp_f32_e32 v131, v85
	v_sub_f32_e32 v85, v130, v82
	v_add_f32_e32 v84, v133, v84
	v_exp_f32_e32 v136, v85
	v_sub_f32_e32 v85, v125, v82
	v_add_f32_e32 v84, v129, v84
	v_exp_f32_e32 v135, v85
	v_sub_f32_e32 v85, v124, v82
	v_add_f32_e32 v84, v128, v84
	v_exp_f32_e32 v137, v85
	v_sub_f32_e32 v85, v127, v82
	v_add_f32_e32 v84, v131, v84
	v_exp_f32_e32 v124, v85
	v_sub_f32_e32 v85, v126, v82
	v_add_f32_e32 v84, v136, v84
	v_exp_f32_e32 v126, v85
	v_sub_f32_e32 v85, v121, v82
	v_add_f32_e32 v84, v135, v84
	v_exp_f32_e32 v125, v85
	v_sub_f32_e32 v85, v120, v82
	v_add_f32_e32 v84, v137, v84
	v_exp_f32_e32 v127, v85
	v_sub_f32_e32 v85, v123, v82
	v_add_f32_e32 v84, v124, v84
	v_exp_f32_e32 v123, v85
	v_sub_f32_e32 v85, v122, v82
	v_add_f32_e32 v84, v126, v84
	v_exp_f32_e32 v130, v85
	v_sub_f32_e32 v85, v117, v82
	v_add_f32_e32 v84, v125, v84
	v_exp_f32_e32 v122, v85
	v_sub_f32_e32 v85, v116, v82
	v_add_f32_e32 v84, v127, v84
	v_exp_f32_e32 v134, v85
	v_sub_f32_e32 v85, v119, v82
	v_add_f32_e32 v84, v123, v84
	v_exp_f32_e32 v108, v85
	v_sub_f32_e32 v85, v118, v82
	v_add_f32_e32 v84, v130, v84
	v_exp_f32_e32 v113, v85
	v_sub_f32_e32 v85, v147, v82
	v_add_f32_e32 v84, v122, v84
	v_exp_f32_e32 v110, v85
	v_sub_f32_e32 v85, v112, v82
	v_add_f32_e32 v84, v134, v84
	v_exp_f32_e32 v115, v85
	v_sub_f32_e32 v85, v192, v82
	v_add_f32_e32 v84, v108, v84
	v_exp_f32_e32 v117, v85
	v_sub_f32_e32 v85, v114, v82
	v_add_f32_e32 v84, v113, v84
	v_exp_f32_e32 v120, v85
	v_sub_f32_e32 v85, v193, v82
	v_add_f32_e32 v84, v110, v84
	v_exp_f32_e32 v119, v85
	v_sub_f32_e32 v85, v109, v82
	v_add_f32_e32 v84, v115, v84
	v_exp_f32_e32 v121, v85
	v_sub_f32_e32 v85, v194, v82
	v_add_f32_e32 v84, v117, v84
	v_exp_f32_e32 v106, v85
	v_sub_f32_e32 v85, v111, v82
	v_add_f32_e32 v84, v120, v84
	v_exp_f32_e32 v109, v85
	v_sub_f32_e32 v85, v105, v82
	v_add_f32_e32 v84, v119, v84
	v_exp_f32_e32 v107, v85
	v_sub_f32_e32 v85, v104, v82
	v_add_f32_e32 v84, v121, v84
	v_exp_f32_e32 v111, v85
	v_sub_f32_e32 v85, v196, v82
	v_add_f32_e32 v84, v106, v84
	v_exp_f32_e32 v112, v85
	v_sub_f32_e32 v85, v195, v82
	v_add_f32_e32 v84, v109, v84
	v_exp_f32_e32 v116, v85
	v_sub_f32_e32 v85, v97, v82
	v_add_f32_e32 v84, v107, v84
	v_exp_f32_e32 v114, v85
	v_sub_f32_e32 v85, v96, v82
	v_add_f32_e32 v84, v111, v84
	v_exp_f32_e32 v118, v85
	v_add_f32_e32 v84, v112, v84
	v_add_f32_e32 v84, v116, v84
	v_add_f32_e32 v84, v114, v84
	v_add_f32_e32 v96, v118, v84
	v_sub_f32_e32 v84, v99, v82
	v_exp_f32_e32 v84, v84
	v_sub_f32_e32 v85, v98, v82
	v_exp_f32_e32 v86, v85
	v_sub_f32_e32 v85, v93, v82
	v_exp_f32_e32 v85, v85
	v_sub_f32_e32 v87, v92, v82
	v_exp_f32_e32 v87, v87
	v_sub_f32_e32 v93, v95, v82
	v_add_f32_e32 v92, v84, v96
	v_exp_f32_e32 v102, v93
	v_sub_f32_e32 v93, v94, v82
	v_add_f32_e32 v92, v86, v92
	v_exp_f32_e32 v104, v93
	v_sub_f32_e32 v89, v89, v82
	v_add_f32_e32 v92, v85, v92
	v_exp_f32_e32 v103, v89
	v_sub_f32_e32 v88, v88, v82
	v_add_f32_e32 v92, v87, v92
	v_exp_f32_e32 v105, v88
	v_sub_f32_e32 v89, v91, v82
	v_add_f32_e32 v88, v102, v92
	v_exp_f32_e32 v94, v89
	v_sub_f32_e32 v89, v90, v82
	v_add_f32_e32 v88, v104, v88
	v_exp_f32_e32 v96, v89
	v_sub_f32_e32 v89, v198, v82
	v_add_f32_e32 v88, v103, v88
	v_exp_f32_e32 v95, v89
	v_sub_f32_e32 v89, v197, v82
	v_add_f32_e32 v88, v105, v88
	v_exp_f32_e32 v97, v89
	v_sub_f32_e32 v89, v202, v82
	v_add_f32_e32 v88, v94, v88
	v_exp_f32_e32 v98, v89
	v_sub_f32_e32 v89, v199, v82
	v_add_f32_e32 v88, v96, v88
	v_exp_f32_e32 v100, v89
	v_sub_f32_e32 v81, v81, v82
	v_add_f32_e32 v88, v95, v88
	v_exp_f32_e32 v99, v81
	v_sub_f32_e32 v80, v80, v82
	v_add_f32_e32 v88, v97, v88
	v_exp_f32_e32 v101, v80
	v_add_f32_e32 v80, v98, v88
	v_add_f32_e32 v80, v100, v80
	v_add_f32_e32 v80, v99, v80
	v_add_f32_e32 v80, v101, v80
	v_mov_b32 v81, v80
	ds_bpermute_b32 v81, v170, v81
	v_bfe_u32 v93, v146, 16, 1
	v_bfe_u32 v82, v191, 16, 1
	v_add3_u32 v92, v191, v82, s94
	v_bfe_u32 v82, v144, 16, 1
	s_waitcnt lgkmcnt(0)
	v_add_f32_e32 v88, v80, v81
	v_add_lshl_u32 v80, s29, v172, 7
	v_bfe_u32 v81, v140, 16, 1
	v_add3_u32 v138, v140, v81, s94
	v_add3_u32 v140, v146, v93, s94
	v_add3_u32 v146, v173, v80, v153
	v_bfe_u32 v81, v83, 16, 1
	v_add_u32_e32 v93, v146, v184
	v_mov_b32 v89, v88
	v_add3_u32 v141, v144, v82, s94
	v_add3_u32 v142, v83, v81, s94
	v_add_u32_e32 v240, v146, v184
	v_add_u32_e32 v241, v146, v185
	v_add_u32_e32 v242, v146, v186
	v_add_u32_e32 v243, v146, v187
	ds_read_b64_tr_b16 v[212:213], v240
	ds_read_b64_tr_b16 v[214:215], v240 offset:2048
	ds_read_b64_tr_b16 v[216:217], v241
	ds_read_b64_tr_b16 v[218:219], v241 offset:2048
	ds_read_b64_tr_b16 v[220:221], v242
	ds_read_b64_tr_b16 v[222:223], v242 offset:2048
	ds_read_b64_tr_b16 v[224:225], v243
	ds_read_b64_tr_b16 v[226:227], v243 offset:2048
	ds_read_b64_tr_b16 v[228:229], v240 offset:8192
	ds_read_b64_tr_b16 v[230:231], v240 offset:10240
	ds_read_b64_tr_b16 v[232:233], v241 offset:8192
	ds_read_b64_tr_b16 v[234:235], v241 offset:10240
	v_bfe_u32 v139, v203, 16, 1
	v_bfe_u32 v90, v145, 16, 1
	v_bfe_u32 v91, v143, 16, 1
	v_add3_u32 v139, v203, v139, s94
	v_add3_u32 v91, v143, v91, s94
	v_add3_u32 v90, v145, v90, s94
	v_lshrrev_b32_e32 v142, 16, v142
	v_lshrrev_b32_e32 v143, 16, v141
	v_lshrrev_b32_e32 v140, 16, v140
	v_lshrrev_b32_e32 v139, 16, v139
	v_and_or_b32 v141, v138, s33, v139
	v_and_or_b32 v140, v92, s33, v140
	v_and_or_b32 v139, v90, s33, v143
	v_and_or_b32 v138, v91, s33, v142
	v_add_u32_e32 v92, v146, v185
	v_add_u32_e32 v91, v146, v186
	s_waitcnt lgkmcnt(10)
	v_mfma_f32_16x16x32_bf16 v[142:145], v[212:215], v[138:141], 0
	ds_read_b64_tr_b16 v[236:237], v242 offset:8192
	ds_read_b64_tr_b16 v[238:239], v242 offset:10240
	v_add_u32_e32 v90, v146, v187
	ds_bpermute_b32 v89, v171, v89
	s_waitcnt lgkmcnt(11)
	v_mfma_f32_16x16x32_bf16 v[192:195], v[216:219], v[138:141], 0
	ds_read_b64_tr_b16 v[212:213], v243 offset:8192
	ds_read_b64_tr_b16 v[214:215], v243 offset:10240
	s_ashr_i32 s29, s28, 31
	s_lshl_b64 s[4:5], s[28:29], 12
	s_waitcnt lgkmcnt(11)
	v_mfma_f32_16x16x32_bf16 v[196:199], v[220:223], v[138:141], 0
	ds_read_b64_tr_b16 v[216:217], v240 offset:16384
	ds_read_b64_tr_b16 v[218:219], v240 offset:18432
	s_lshl_b32 s28, s62, 6
	s_ashr_i32 s29, s28, 31
	s_waitcnt lgkmcnt(11)
	v_mfma_f32_16x16x32_bf16 v[80:83], v[224:227], v[138:141], 0
	ds_read_b64_tr_b16 v[220:221], v241 offset:16384
	ds_read_b64_tr_b16 v[222:223], v241 offset:18432
	v_bfe_u32 v138, v211, 16, 1
	v_bfe_u32 v139, v209, 16, 1
	v_bfe_u32 v140, v207, 16, 1
	v_bfe_u32 v141, v205, 16, 1
	v_add3_u32 v146, v205, v141, s94
	v_add3_u32 v147, v207, v140, s94
	v_add3_u32 v153, v209, v139, s94
	v_add3_u32 v191, v211, v138, s94
	v_bfe_u32 v138, v204, 16, 1
	v_bfe_u32 v139, v206, 16, 1
	v_bfe_u32 v140, v208, 16, 1
	v_bfe_u32 v141, v210, 16, 1
	v_add3_u32 v202, v210, v141, s94
	v_add3_u32 v203, v208, v140, s94
	v_add3_u32 v205, v206, v139, s94
	v_add3_u32 v204, v204, v138, s94
	v_lshrrev_b32_e32 v206, 16, v204
	v_lshrrev_b32_e32 v207, 16, v205
	v_lshrrev_b32_e32 v203, 16, v203
	v_lshrrev_b32_e32 v202, 16, v202
	v_and_or_b32 v205, v191, s33, v202
	v_and_or_b32 v204, v153, s33, v203
	v_and_or_b32 v203, v147, s33, v207
	v_and_or_b32 v202, v146, s33, v206
	v_bfe_u32 v146, v137, 16, 1
	v_bfe_u32 v147, v136, 16, 1
	s_waitcnt lgkmcnt(11)
	v_mfma_f32_16x16x32_bf16 v[138:141], v[228:231], v[202:205], v[142:145]
	ds_read_b64_tr_b16 v[224:225], v242 offset:16384
	ds_read_b64_tr_b16 v[226:227], v242 offset:18432
	s_nop 2
	v_bfe_u32 v153, v128, 16, 1
	v_bfe_u32 v191, v133, 16, 1
	s_waitcnt lgkmcnt(11)
	v_mfma_f32_16x16x32_bf16 v[142:145], v[232:235], v[202:205], v[192:195]
	ds_read_b64_tr_b16 v[228:229], v243 offset:16384
	ds_read_b64_tr_b16 v[230:231], v243 offset:18432
	s_nop 2
	v_add3_u32 v133, v133, v191, s94
	v_add3_u32 v128, v128, v153, s94
	s_waitcnt lgkmcnt(11)
	v_mfma_f32_16x16x32_bf16 v[192:195], v[236:239], v[202:205], v[196:199]
	ds_read_b64_tr_b16 v[232:233], v240 offset:24576
	ds_read_b64_tr_b16 v[234:235], v240 offset:26624
	s_nop 2
	v_add3_u32 v136, v136, v147, s94
	v_add3_u32 v137, v137, v146, s94
	s_waitcnt lgkmcnt(10)
	v_mfma_f32_16x16x32_bf16 v[80:83], v[212:215], v[202:205], v[80:83]
	ds_read_b64_tr_b16 v[236:237], v241 offset:24576
	ds_read_b64_tr_b16 v[238:239], v241 offset:26624
	v_bfe_u32 v146, v132, 16, 1
	v_bfe_u32 v147, v129, 16, 1
	v_bfe_u32 v153, v131, 16, 1
	v_bfe_u32 v191, v135, 16, 1
	v_add3_u32 v135, v135, v191, s94
	v_add3_u32 v131, v131, v153, s94
	v_add3_u32 v129, v129, v147, s94
	v_add3_u32 v132, v132, v146, s94
	v_lshrrev_b32_e32 v132, 16, v132
	v_lshrrev_b32_e32 v129, 16, v129
	v_lshrrev_b32_e32 v131, 16, v131
	v_lshrrev_b32_e32 v135, 16, v135
	v_and_or_b32 v205, v137, s33, v135
	v_and_or_b32 v204, v136, s33, v131
	v_and_or_b32 v203, v128, s33, v129
	v_and_or_b32 v202, v133, s33, v132
	v_bfe_u32 v129, v130, 16, 1
	v_bfe_u32 v131, v127, 16, 1
	s_waitcnt lgkmcnt(10)
	v_mfma_f32_16x16x32_bf16 v[136:139], v[216:219], v[202:205], v[138:141]
	ds_read_b64_tr_b16 v[212:213], v242 offset:24576
	ds_read_b64_tr_b16 v[214:215], v242 offset:26624
	v_bfe_u32 v132, v126, 16, 1
	v_add3_u32 v126, v126, v132, s94
	s_waitcnt lgkmcnt(10)
	v_mfma_f32_16x16x32_bf16 v[140:143], v[220:223], v[202:205], v[142:145]
	ds_read_b64_tr_b16 v[216:217], v243 offset:24576
	ds_read_b64_tr_b16 v[218:219], v243 offset:26624
	s_nop 2
	v_add3_u32 v127, v127, v131, s94
	v_add3_u32 v130, v130, v129, s94
	v_bfe_u32 v129, v124, 16, 1
	v_bfe_u32 v131, v125, 16, 1
	v_bfe_u32 v132, v123, 16, 1
	v_bfe_u32 v133, v122, 16, 1
	v_bfe_u32 v128, v134, 16, 1
	v_add3_u32 v133, v122, v133, s94
	v_add3_u32 v132, v123, v132, s94
	v_add3_u32 v131, v125, v131, s94
	v_add3_u32 v129, v124, v129, s94
	v_add3_u32 v128, v134, v128, s94
	v_lshrrev_b32_e32 v134, 16, v129
	v_lshrrev_b32_e32 v131, 16, v131
	v_lshrrev_b32_e32 v132, 16, v132
	v_lshrrev_b32_e32 v129, 16, v133
	s_waitcnt lgkmcnt(10)
	v_mfma_f32_16x16x32_bf16 v[144:147], v[224:227], v[202:205], v[192:195]
	ds_read_b64_tr_b16 v[220:221], v240 offset:32768
	ds_read_b64_tr_b16 v[222:223], v240 offset:34816
	s_nop 2
	v_and_or_b32 v129, v128, s33, v129
	v_and_or_b32 v128, v130, s33, v132
	v_and_or_b32 v127, v127, s33, v131
	v_and_or_b32 v126, v126, s33, v134
	s_waitcnt lgkmcnt(10)
	v_mfma_f32_16x16x32_bf16 v[80:83], v[228:231], v[202:205], v[80:83]
	ds_read_b64_tr_b16 v[224:225], v241 offset:32768
	ds_read_b64_tr_b16 v[226:227], v241 offset:34816
	s_add_u32 s28, s4, s28
	s_addc_u32 s29, s5, s29
	s_add_i32 s58, s58, s59
	s_waitcnt lgkmcnt(10)
	v_mfma_f32_16x16x32_bf16 v[122:125], v[232:235], v[126:129], v[136:139]
	ds_read_b64_tr_b16 v[228:229], v242 offset:32768
	ds_read_b64_tr_b16 v[230:231], v242 offset:34816
	s_nop 1
	s_waitcnt lgkmcnt(10)
	v_mfma_f32_16x16x32_bf16 v[130:133], v[236:239], v[126:129], v[140:143]
	ds_read_b64_tr_b16 v[232:233], v240 offset:40960
	ds_read_b64_tr_b16 v[234:235], v240 offset:43008
	s_nop 1
	s_waitcnt lgkmcnt(10)
	v_mfma_f32_16x16x32_bf16 v[134:137], v[212:215], v[126:129], v[144:147]
	ds_read_b64_tr_b16 v[236:237], v241 offset:40960
	ds_read_b64_tr_b16 v[238:239], v241 offset:43008
	s_waitcnt lgkmcnt(10)
	v_mfma_f32_16x16x32_bf16 v[80:83], v[216:219], v[126:129], v[80:83]
	ds_read_b64_tr_b16 v[212:213], v243 offset:32768
	ds_read_b64_tr_b16 v[214:215], v243 offset:34816
	v_bfe_u32 v126, v121, 16, 1
	v_bfe_u32 v127, v120, 16, 1
	v_bfe_u32 v128, v115, 16, 1
	v_bfe_u32 v129, v113, 16, 1
	v_add3_u32 v113, v113, v129, s94
	v_add3_u32 v115, v115, v128, s94
	v_add3_u32 v120, v120, v127, s94
	v_add3_u32 v121, v121, v126, s94
	v_bfe_u32 v126, v108, 16, 1
	v_bfe_u32 v127, v110, 16, 1
	v_bfe_u32 v128, v117, 16, 1
	v_bfe_u32 v129, v119, 16, 1
	v_add3_u32 v119, v119, v129, s94
	v_add3_u32 v117, v117, v128, s94
	v_add3_u32 v110, v110, v127, s94
	v_add3_u32 v108, v108, v126, s94
	v_lshrrev_b32_e32 v108, 16, v108
	v_lshrrev_b32_e32 v110, 16, v110
	v_lshrrev_b32_e32 v117, 16, v117
	v_lshrrev_b32_e32 v119, 16, v119
	v_and_or_b32 v141, v121, s33, v119
	v_and_or_b32 v140, v120, s33, v117
	v_and_or_b32 v139, v115, s33, v110
	v_and_or_b32 v138, v113, s33, v108
	v_bfe_u32 v108, v118, 16, 1
	v_bfe_u32 v110, v116, 16, 1
	s_waitcnt lgkmcnt(10)
	v_mfma_f32_16x16x32_bf16 v[120:123], v[220:223], v[138:141], v[122:125]
	ds_read_b64_tr_b16 v[216:217], v242 offset:40960
	ds_read_b64_tr_b16 v[218:219], v242 offset:43008
	s_nop 2
	v_bfe_u32 v113, v111, 16, 1
	v_bfe_u32 v115, v109, 16, 1
	s_waitcnt lgkmcnt(10)
	v_mfma_f32_16x16x32_bf16 v[124:127], v[224:227], v[138:141], v[130:133]
	ds_read_b64_tr_b16 v[220:221], v243 offset:40960
	ds_read_b64_tr_b16 v[222:223], v243 offset:43008
	s_nop 1
	v_add3_u32 v115, v109, v115, s94
	v_add3_u32 v111, v111, v113, s94
	v_add3_u32 v110, v116, v110, s94
	v_add3_u32 v113, v118, v108, s94
	v_bfe_u32 v108, v106, 16, 1
	v_bfe_u32 v109, v107, 16, 1
	v_bfe_u32 v116, v112, 16, 1
	v_bfe_u32 v117, v114, 16, 1
	v_add3_u32 v114, v114, v117, s94
	v_add3_u32 v112, v112, v116, s94
	v_add3_u32 v116, v107, v109, s94
	v_add3_u32 v117, v106, v108, s94
	v_lshrrev_b32_e32 v117, 16, v117
	v_lshrrev_b32_e32 v116, 16, v116
	v_lshrrev_b32_e32 v112, 16, v112
	v_lshrrev_b32_e32 v114, 16, v114
	s_waitcnt lgkmcnt(10)
	v_mfma_f32_16x16x32_bf16 v[128:131], v[228:231], v[138:141], v[134:137]
	ds_read_b64_tr_b16 v[224:225], v240 offset:49152
	ds_read_b64_tr_b16 v[226:227], v240 offset:51200
	s_nop 1
	v_and_or_b32 v113, v113, s33, v114
	v_and_or_b32 v112, v110, s33, v112
	v_and_or_b32 v111, v111, s33, v116
	v_and_or_b32 v110, v115, s33, v117
	s_waitcnt lgkmcnt(10)
	s_nop 0
	v_mfma_f32_16x16x32_bf16 v[106:109], v[232:235], v[110:113], v[120:123]
	ds_read_b64_tr_b16 v[228:229], v241 offset:49152
	ds_read_b64_tr_b16 v[230:231], v241 offset:51200
	s_nop 1
	s_waitcnt lgkmcnt(10)
	v_mfma_f32_16x16x32_bf16 v[114:117], v[236:239], v[110:113], v[124:127]
	ds_read_b64_tr_b16 v[232:233], v242 offset:49152
	ds_read_b64_tr_b16 v[234:235], v242 offset:51200
	s_nop 1
	s_waitcnt lgkmcnt(10)
	v_mfma_f32_16x16x32_bf16 v[80:83], v[212:215], v[138:141], v[80:83]
	ds_read_b64_tr_b16 v[236:237], v243 offset:49152
	ds_read_b64_tr_b16 v[238:239], v243 offset:51200
	s_waitcnt lgkmcnt(10)
	v_mfma_f32_16x16x32_bf16 v[118:121], v[216:219], v[110:113], v[128:131]
	ds_read_b64_tr_b16 v[212:213], v240 offset:57344
	ds_read_b64_tr_b16 v[214:215], v240 offset:59392
	s_waitcnt lgkmcnt(10)
	v_mfma_f32_16x16x32_bf16 v[80:83], v[220:223], v[110:113], v[80:83]
	ds_read_b64_tr_b16 v[216:217], v241 offset:57344
	ds_read_b64_tr_b16 v[218:219], v241 offset:59392
	v_bfe_u32 v110, v105, 16, 1
	v_bfe_u32 v111, v104, 16, 1
	v_bfe_u32 v112, v87, 16, 1
	v_bfe_u32 v113, v86, 16, 1
	v_add3_u32 v122, v86, v113, s94
	v_add3_u32 v123, v87, v112, s94
	v_add3_u32 v111, v104, v111, s94
	v_add3_u32 v110, v105, v110, s94
	v_bfe_u32 v86, v84, 16, 1
	v_bfe_u32 v87, v85, 16, 1
	v_bfe_u32 v104, v102, 16, 1
	v_bfe_u32 v105, v103, 16, 1
	v_add3_u32 v103, v103, v105, s94
	v_add3_u32 v102, v102, v104, s94
	v_add3_u32 v85, v85, v87, s94
	v_add3_u32 v84, v84, v86, s94
	v_lshrrev_b32_e32 v124, 16, v84
	v_lshrrev_b32_e32 v125, 16, v85
	v_lshrrev_b32_e32 v112, 16, v102
	v_lshrrev_b32_e32 v113, 16, v103
	v_and_or_b32 v113, v110, s33, v113
	v_and_or_b32 v112, v111, s33, v112
	v_and_or_b32 v111, v123, s33, v125
	v_and_or_b32 v110, v122, s33, v124
	s_nop 0
	s_waitcnt lgkmcnt(10)
	v_mfma_f32_16x16x32_bf16 v[106:109], v[224:227], v[110:113], v[106:109]
	ds_read_b64_tr_b16 v[220:221], v242 offset:57344
	ds_read_b64_tr_b16 v[222:223], v242 offset:59392
	s_waitcnt lgkmcnt(10)
	v_mfma_f32_16x16x32_bf16 v[102:105], v[228:231], v[110:113], v[114:117]
	ds_read_b64_tr_b16 v[224:225], v243 offset:57344
	ds_read_b64_tr_b16 v[226:227], v243 offset:59392
	s_nop 2
	s_waitcnt lgkmcnt(10)
	v_mfma_f32_16x16x32_bf16 v[84:87], v[232:235], v[110:113], v[118:121]
	s_waitcnt lgkmcnt(8)
	v_mfma_f32_16x16x32_bf16 v[80:83], v[236:239], v[110:113], v[80:83]
	v_bfe_u32 v112, v97, 16, 1
	v_bfe_u32 v113, v96, 16, 1
	v_add3_u32 v114, v96, v113, s94
	v_add3_u32 v115, v97, v112, s94
	v_bfe_u32 v96, v94, 16, 1
	v_bfe_u32 v97, v95, 16, 1
	v_add3_u32 v95, v95, v97, s94
	v_add3_u32 v94, v94, v96, s94
	v_bfe_u32 v110, v101, 16, 1
	v_bfe_u32 v111, v100, 16, 1
	v_lshrrev_b32_e32 v116, 16, v94
	v_lshrrev_b32_e32 v117, 16, v95
	v_add3_u32 v100, v100, v111, s94
	v_add3_u32 v101, v101, v110, s94
	v_bfe_u32 v110, v98, 16, 1
	v_bfe_u32 v111, v99, 16, 1
	v_add3_u32 v99, v99, v111, s94
	v_add3_u32 v98, v98, v110, s94
	v_lshrrev_b32_e32 v98, 16, v98
	v_lshrrev_b32_e32 v99, 16, v99
	v_and_or_b32 v101, v101, s33, v99
	v_and_or_b32 v100, v100, s33, v98
	v_and_or_b32 v99, v115, s33, v117
	v_and_or_b32 v98, v114, s33, v116
	s_waitcnt lgkmcnt(6)
	s_nop 0
	v_mfma_f32_16x16x32_bf16 v[92:95], v[212:215], v[98:101], v[106:109]
	s_nop 2
	v_add_f32_e32 v90, v88, v89
	v_div_scale_f32 v91, s[4:5], v90, v90, 1.0
	v_rcp_f32_e32 v96, v91
	s_waitcnt lgkmcnt(4)
	v_mfma_f32_16x16x32_bf16 v[102:105], v[216:219], v[98:101], v[102:105]
	v_mov_b32_e32 v89, s29
	v_or_b32_e32 v88, s28, v150
	v_fma_f32 v97, -v91, v96, 1.0
	v_fmac_f32_e32 v96, v97, v96
	v_div_scale_f32 v97, vcc, 1.0, v90, 1.0
	s_waitcnt lgkmcnt(2)
	v_mfma_f32_16x16x32_bf16 v[84:87], v[220:223], v[98:101], v[84:87]
	v_lshlrev_b64 v[88:89], 10, v[88:89]
	s_and_b32 s4, s61, 0xffffffc0
	v_lshl_add_u64 v[88:89], s[6:7], 0, v[88:89]
	s_waitcnt lgkmcnt(0)
	v_mfma_f32_16x16x32_bf16 v[80:83], v[224:227], v[98:101], v[80:83]
	v_mul_f32_e32 v98, v97, v96
	v_fma_f32 v99, -v91, v98, v97
	v_fmac_f32_e32 v98, v99, v96
	v_fma_f32 v91, -v91, v98, v97
	v_div_fmas_f32 v91, v91, v96, v98
	v_div_fixup_f32 v90, v91, v90, 1.0
	v_mul_f32_e32 v91, v90, v92
	v_mul_f32_e32 v92, v90, v93
	v_mov_b32_e32 v93, v245
	v_cvt_pk_fp8_f32 v93, v91, v92
	v_mul_f32_e32 v91, v90, v94
	v_mul_f32_e32 v92, v90, v95
	v_mul_f32_e32 v94, v90, v102
	v_mul_f32_e32 v95, v90, v103
	v_mov_b32_e32 v96, v245
	v_cvt_pk_fp8_f32 v96, v94, v95
	v_cvt_pk_fp8_f32 v93, v91, v92 op_sel:[0,0,1]
	v_mul_f32_e32 v91, v90, v104
	v_mul_f32_e32 v92, v90, v105
	v_cvt_pk_fp8_f32 v96, v91, v92 op_sel:[0,0,1]
	v_mul_f32_e32 v84, v90, v84
	v_mul_f32_e32 v85, v90, v85
	v_mov_b32_e32 v91, v245
	v_cvt_pk_fp8_f32 v91, v84, v85
	v_mul_f32_e32 v84, v90, v86
	v_mul_f32_e32 v80, v90, v80
	v_mul_f32_e32 v81, v90, v81
	v_mov_b32_e32 v86, v245
	v_cvt_pk_fp8_f32 v86, v80, v81
	s_ashr_i32 s5, s4, 31
	v_mul_f32_e32 v85, v90, v87
	v_mul_f32_e32 v80, v90, v82
	v_mul_f32_e32 v81, v90, v83
	v_lshl_add_u64 v[88:89], v[88:89], 0, s[4:5]
	v_cvt_pk_fp8_f32 v91, v84, v85 op_sel:[0,0,1]
	v_cvt_pk_fp8_f32 v86, v80, v81 op_sel:[0,0,1]
	s_waitcnt vmcnt(0)
	v_mov_b64_e32 v[82:83], v[78:79]
	v_mov_b64_e32 v[102:103], v[74:75]
	v_lshl_add_u64 v[88:89], v[88:89], 0, v[148:149]
	s_andn2_b64 vcc, exec, s[26:27]
	v_mov_b64_e32 v[80:81], v[76:77]
	v_mov_b64_e32 v[100:101], v[72:73]
	v_mov_b32_e32 v240, v93
	v_mov_b32_e32 v241, v96
	v_mov_b32_e32 v242, v91
	v_mov_b32_e32 v243, v86
	v_mbcnt_lo_u32_b32 v236, -1, 0
	v_mbcnt_hi_u32_b32 v236, -1, v236
	v_lshrrev_b32_e32 v236, 4, v236
	v_mul_u32_u24_e32 v236, 12, v236
	v_mov_b32_e32 v237, v245
	v_permlane16_swap_b32_e32 v240, v241
	v_permlane16_swap_b32_e32 v242, v243
	v_lshl_add_u64 v[238:239], v[88:89], 0, v[236:237]
	s_nop 0
	v_permlane32_swap_b32_e32 v240, v242
	v_permlane32_swap_b32_e32 v241, v243
	global_store_dwordx4 v[238:239], v[240:243], off
	s_cbranch_vccz .LBB0_752

.LBB0_624:
	s_add_i32 s62, s62, s55
	s_min_u32 s4, s34, 60
	v_med3_i32 v191, s62, 4, 60
	v_subrev_u32_e32 v84, s4, v191
	v_lshlrev_b32_e32 v153, 13, v84
	v_add_u16_e32 v86, s29, v154
	v_add_u32_e32 v85, s29, v154
	v_add_u32_e32 v84, 0, v153
	v_lshrrev_b16_e32 v88, 1, v86
	v_bitop3_b32 v86, v88, v155, 7 bitop3:0x6c
	v_lshl_add_u32 v89, v85, 7, v84
	v_lshl_add_u32 v196, v86, 4, v89
	v_bitop3_b32 v88, v88, v183, 7 bitop3:0x6c
	v_lshl_add_u32 v197, v88, 4, v89
	s_movk_i32 s4, 0x7c
	ds_read_b128 v[212:215], v196
	ds_read_b128 v[216:219], v197
	ds_read_b128 v[220:223], v196 offset:2048
	ds_read_b128 v[224:227], v197 offset:2048
	ds_read_b128 v[228:231], v196 offset:8192
	ds_read_b128 v[232:235], v197 offset:8192
	ds_read_b128 v[236:239], v196 offset:10240
	ds_read_b128 v[240:243], v197 offset:10240
	s_waitcnt lgkmcnt(6)
	v_mfma_f32_16x16x32_bf16 v[144:147], v[212:215], v[100:103], 0
	v_mfma_f32_16x16x32_bf16 v[144:147], v[216:219], v[80:83], v[144:147]
	ds_read_b128 v[212:215], v196 offset:16384
	ds_read_b128 v[216:219], v197 offset:16384
	s_waitcnt lgkmcnt(6)
	v_mfma_f32_16x16x32_bf16 v[140:143], v[220:223], v[100:103], 0
	v_mfma_f32_16x16x32_bf16 v[140:143], v[224:227], v[80:83], v[140:143]
	ds_read_b128 v[220:223], v196 offset:18432
	ds_read_b128 v[224:227], v197 offset:18432
	s_waitcnt lgkmcnt(6)
	v_mfma_f32_16x16x32_bf16 v[136:139], v[228:231], v[100:103], 0
	v_mfma_f32_16x16x32_bf16 v[136:139], v[232:235], v[80:83], v[136:139]
	ds_read_b128 v[228:231], v196 offset:24576
	ds_read_b128 v[232:235], v197 offset:24576
	s_waitcnt lgkmcnt(6)
	v_mfma_f32_16x16x32_bf16 v[132:135], v[236:239], v[100:103], 0
	v_mfma_f32_16x16x32_bf16 v[132:135], v[240:243], v[80:83], v[132:135]
	ds_read_b128 v[236:239], v196 offset:26624
	ds_read_b128 v[240:243], v197 offset:26624
	s_waitcnt lgkmcnt(6)
	v_mfma_f32_16x16x32_bf16 v[128:131], v[212:215], v[100:103], 0
	v_mfma_f32_16x16x32_bf16 v[128:131], v[216:219], v[80:83], v[128:131]
	ds_read_b128 v[212:215], v196 offset:32768
	ds_read_b128 v[216:219], v197 offset:32768
	s_waitcnt lgkmcnt(6)
	v_mfma_f32_16x16x32_bf16 v[124:127], v[220:223], v[100:103], 0
	v_mfma_f32_16x16x32_bf16 v[124:127], v[224:227], v[80:83], v[124:127]
	ds_read_b128 v[220:223], v196 offset:34816
	ds_read_b128 v[224:227], v197 offset:34816
	s_waitcnt lgkmcnt(6)
	v_mfma_f32_16x16x32_bf16 v[120:123], v[228:231], v[100:103], 0
	v_mfma_f32_16x16x32_bf16 v[120:123], v[232:235], v[80:83], v[120:123]
	ds_read_b128 v[228:231], v196 offset:40960
	ds_read_b128 v[232:235], v197 offset:40960
	s_waitcnt lgkmcnt(6)
	v_mfma_f32_16x16x32_bf16 v[116:119], v[236:239], v[100:103], 0
	v_mfma_f32_16x16x32_bf16 v[116:119], v[240:243], v[80:83], v[116:119]
	ds_read_b128 v[236:239], v196 offset:43008
	ds_read_b128 v[240:243], v197 offset:43008
	s_waitcnt lgkmcnt(6)
	v_mfma_f32_16x16x32_bf16 v[112:115], v[212:215], v[100:103], 0
	v_mfma_f32_16x16x32_bf16 v[112:115], v[216:219], v[80:83], v[112:115]
	ds_read_b128 v[212:215], v196 offset:49152
	ds_read_b128 v[216:219], v197 offset:49152
	s_waitcnt lgkmcnt(6)
	v_mfma_f32_16x16x32_bf16 v[108:111], v[220:223], v[100:103], 0
	v_mfma_f32_16x16x32_bf16 v[108:111], v[224:227], v[80:83], v[108:111]
	ds_read_b128 v[220:223], v196 offset:51200
	ds_read_b128 v[224:227], v197 offset:51200
	s_waitcnt lgkmcnt(6)
	v_mfma_f32_16x16x32_bf16 v[104:107], v[228:231], v[100:103], 0
	v_mfma_f32_16x16x32_bf16 v[104:107], v[232:235], v[80:83], v[104:107]
	ds_read_b128 v[228:231], v196 offset:57344
	ds_read_b128 v[232:235], v197 offset:57344
	s_waitcnt lgkmcnt(6)
	v_mfma_f32_16x16x32_bf16 v[96:99], v[236:239], v[100:103], 0
	v_mfma_f32_16x16x32_bf16 v[96:99], v[240:243], v[80:83], v[96:99]
	ds_read_b128 v[236:239], v196 offset:59392
	ds_read_b128 v[240:243], v197 offset:59392
	s_waitcnt lgkmcnt(6)
	v_mfma_f32_16x16x32_bf16 v[92:95], v[212:215], v[100:103], 0
	v_mfma_f32_16x16x32_bf16 v[92:95], v[216:219], v[80:83], v[92:95]
	s_waitcnt lgkmcnt(4)
	v_mfma_f32_16x16x32_bf16 v[88:91], v[220:223], v[100:103], 0
	v_mfma_f32_16x16x32_bf16 v[88:91], v[224:227], v[80:83], v[88:91]
	s_waitcnt lgkmcnt(2)
	v_mfma_f32_16x16x32_bf16 v[84:87], v[228:231], v[100:103], 0
	v_mfma_f32_16x16x32_bf16 v[84:87], v[232:235], v[80:83], v[84:87]
	s_waitcnt lgkmcnt(0)
	v_mfma_f32_16x16x32_bf16 v[192:195], v[236:239], v[100:103], 0
	v_mfma_f32_16x16x32_bf16 v[80:83], v[240:243], v[80:83], v[192:195]
	v_add_u32_e32 v246, s29, v148
	v_subrev_u32_e32 v247, s62, v191
	v_mul_lo_u32 v247, v247, s4
	v_sub_u32_e32 v248, v246, v150
	v_lshl_add_u32 v247, v248, 2, v247
	v_add_u32_e32 v247, 0x23e10, v247
	v_cmp_ge_u32_e32 vcc, v246, v188
	v_cmp_lt_u32_e64 s[4:5], v246, v189
	s_and_b64 s[30:31], vcc, s[4:5]
	v_or_b32_e32 v248, 1, v246
	v_cmp_ge_u32_e32 vcc, v248, v188
	v_cmp_lt_u32_e64 s[4:5], v248, v189
	s_and_b64 s[34:35], vcc, s[4:5]
	v_or_b32_e32 v248, 2, v246
	v_cmp_ge_u32_e32 vcc, v248, v188
	v_cmp_lt_u32_e64 s[4:5], v248, v189
	s_and_b64 s[36:37], vcc, s[4:5]
	v_or_b32_e32 v248, 3, v246
	v_cmp_ge_u32_e32 vcc, v248, v188
	v_cmp_lt_u32_e64 s[4:5], v248, v189
	s_and_b64 s[38:39], vcc, s[4:5]
	v_add_u32_e32 v248, 16, v246
	v_cmp_ge_u32_e32 vcc, v248, v188
	v_cmp_lt_u32_e64 s[4:5], v248, v189
	s_and_b64 s[40:41], vcc, s[4:5]
	v_add_u32_e32 v248, 17, v246
	v_cmp_ge_u32_e32 vcc, v248, v188
	v_cmp_lt_u32_e64 s[4:5], v248, v189
	s_and_b64 s[42:43], vcc, s[4:5]
	v_add_u32_e32 v248, 18, v246
	v_cmp_ge_u32_e32 vcc, v248, v188
	v_cmp_lt_u32_e64 s[4:5], v248, v189
	s_and_b64 s[44:45], vcc, s[4:5]
	v_add_u32_e32 v248, 19, v246
	v_cmp_ge_u32_e32 vcc, v248, v188
	v_cmp_lt_u32_e64 s[4:5], v248, v189
	s_and_b64 s[4:5], vcc, s[4:5]
	v_mov_b32_e32 v248, 64
	v_mov_b32_e32 v249, 0xff800000
	v_cndmask_b32_e64 v250, v248, 0, s[30:31]
	v_cndmask_b32_e64 v251, v248, 0, s[34:35]
	v_cndmask_b32_e64 v252, v248, 0, s[36:37]
	v_cndmask_b32_e64 v246, v248, 0, s[38:39]
	v_add3_u32 v250, v250, v247, 0
	v_add3_u32 v251, v251, v247, 4
	v_add3_u32 v252, v252, v247, 8
	v_add3_u32 v246, v246, v247, 12
	ds_read_b32 v212, v250 offset:928
	ds_read_b32 v213, v251 offset:928
	ds_read_b32 v214, v252 offset:928
	ds_read_b32 v215, v246 offset:928
	ds_read_b32 v216, v250 offset:1052
	ds_read_b32 v217, v251 offset:1052
	ds_read_b32 v218, v252 offset:1052
	ds_read_b32 v219, v246 offset:1052
	ds_read_b32 v220, v250 offset:1176
	ds_read_b32 v221, v251 offset:1176
	ds_read_b32 v222, v252 offset:1176
	ds_read_b32 v223, v246 offset:1176
	ds_read_b32 v224, v250 offset:1300
	ds_read_b32 v225, v251 offset:1300
	ds_read_b32 v226, v252 offset:1300
	ds_read_b32 v227, v246 offset:1300
	ds_read_b32 v228, v250 offset:1424
	ds_read_b32 v229, v251 offset:1424
	ds_read_b32 v230, v252 offset:1424
	ds_read_b32 v231, v246 offset:1424
	ds_read_b32 v232, v250 offset:1548
	ds_read_b32 v233, v251 offset:1548
	ds_read_b32 v234, v252 offset:1548
	ds_read_b32 v235, v246 offset:1548
	ds_read_b32 v236, v250 offset:1672
	ds_read_b32 v237, v251 offset:1672
	ds_read_b32 v238, v252 offset:1672
	ds_read_b32 v239, v246 offset:1672
	ds_read_b32 v240, v250 offset:1796
	ds_read_b32 v241, v251 offset:1796
	ds_read_b32 v242, v252 offset:1796
	ds_read_b32 v243, v246 offset:1796
	s_waitcnt lgkmcnt(15)
	v_add_f32_e32 v101, v144, v212
	v_cndmask_b32_e64 v101, v249, v101, s[30:31]
	v_add_f32_e32 v100, v145, v213
	v_cndmask_b32_e64 v100, v249, v100, s[34:35]
	v_add_f32_e32 v103, v146, v214
	v_cndmask_b32_e64 v103, v249, v103, s[36:37]
	v_add_f32_e32 v102, v147, v215
	v_cndmask_b32_e64 v102, v249, v102, s[38:39]
	v_add_f32_e32 v145, v140, v212
	v_cndmask_b32_e64 v145, v249, v145, s[40:41]
	v_add_f32_e32 v144, v141, v213
	v_cndmask_b32_e64 v144, v249, v144, s[42:43]
	v_add_f32_e32 v146, v142, v214
	v_cndmask_b32_e64 v146, v249, v146, s[44:45]
	v_add_f32_e32 v140, v143, v215
	v_cndmask_b32_e64 v140, v249, v140, s[4:5]
	s_waitcnt lgkmcnt(15)
	v_add_f32_e32 v142, v136, v216
	v_cndmask_b32_e64 v142, v249, v142, s[30:31]
	v_add_f32_e32 v141, v137, v217
	v_cndmask_b32_e64 v141, v249, v141, s[34:35]
	v_add_f32_e32 v137, v138, v218
	v_cndmask_b32_e64 v137, v249, v137, s[36:37]
	v_add_f32_e32 v136, v139, v219
	v_cndmask_b32_e64 v136, v249, v136, s[38:39]
	v_add_f32_e32 v139, v132, v216
	v_cndmask_b32_e64 v139, v249, v139, s[40:41]
	v_add_f32_e32 v138, v133, v217
	v_cndmask_b32_e64 v138, v249, v138, s[42:43]
	v_add_f32_e32 v133, v134, v218
	v_cndmask_b32_e64 v133, v249, v133, s[44:45]
	v_add_f32_e32 v132, v135, v219
	v_cndmask_b32_e64 v132, v249, v132, s[4:5]
	s_waitcnt lgkmcnt(15)
	v_add_f32_e32 v135, v128, v220
	v_cndmask_b32_e64 v135, v249, v135, s[30:31]
	v_add_f32_e32 v134, v129, v221
	v_cndmask_b32_e64 v134, v249, v134, s[34:35]
	v_add_f32_e32 v129, v130, v222
	v_cndmask_b32_e64 v129, v249, v129, s[36:37]
	v_add_f32_e32 v128, v131, v223
	v_cndmask_b32_e64 v128, v249, v128, s[38:39]
	v_add_f32_e32 v131, v124, v220
	v_cndmask_b32_e64 v131, v249, v131, s[40:41]
	v_add_f32_e32 v130, v125, v221
	v_cndmask_b32_e64 v130, v249, v130, s[42:43]
	v_add_f32_e32 v125, v126, v222
	v_cndmask_b32_e64 v125, v249, v125, s[44:45]
	v_add_f32_e32 v124, v127, v223
	v_cndmask_b32_e64 v124, v249, v124, s[4:5]
	s_waitcnt lgkmcnt(15)
	v_add_f32_e32 v127, v120, v224
	v_cndmask_b32_e64 v127, v249, v127, s[30:31]
	v_add_f32_e32 v126, v121, v225
	v_cndmask_b32_e64 v126, v249, v126, s[34:35]
	v_add_f32_e32 v121, v122, v226
	v_cndmask_b32_e64 v121, v249, v121, s[36:37]
	v_add_f32_e32 v120, v123, v227
	v_cndmask_b32_e64 v120, v249, v120, s[38:39]
	v_add_f32_e32 v123, v116, v224
	v_cndmask_b32_e64 v123, v249, v123, s[40:41]
	v_add_f32_e32 v122, v117, v225
	v_cndmask_b32_e64 v122, v249, v122, s[42:43]
	v_add_f32_e32 v117, v118, v226
	v_cndmask_b32_e64 v117, v249, v117, s[44:45]
	v_add_f32_e32 v116, v119, v227
	v_cndmask_b32_e64 v116, v249, v116, s[4:5]
	s_waitcnt lgkmcnt(12)
	v_add_f32_e32 v119, v112, v228
	v_cndmask_b32_e64 v119, v249, v119, s[30:31]
	v_add_f32_e32 v118, v113, v229
	v_cndmask_b32_e64 v118, v249, v118, s[34:35]
	v_add_f32_e32 v147, v114, v230
	v_cndmask_b32_e64 v147, v249, v147, s[36:37]
	v_add_f32_e32 v112, v115, v231
	v_cndmask_b32_e64 v112, v249, v112, s[38:39]
	v_add_f32_e32 v192, v108, v228
	v_cndmask_b32_e64 v192, v249, v192, s[40:41]
	v_add_f32_e32 v114, v109, v229
	v_cndmask_b32_e64 v114, v249, v114, s[42:43]
	v_add_f32_e32 v193, v110, v230
	v_cndmask_b32_e64 v193, v249, v193, s[44:45]
	v_add_f32_e32 v109, v111, v231
	v_cndmask_b32_e64 v109, v249, v109, s[4:5]
	s_waitcnt lgkmcnt(8)
	v_add_f32_e32 v194, v104, v232
	v_cndmask_b32_e64 v194, v249, v194, s[30:31]
	v_add_f32_e32 v111, v105, v233
	v_cndmask_b32_e64 v111, v249, v111, s[34:35]
	v_add_f32_e32 v105, v106, v234
	v_cndmask_b32_e64 v105, v249, v105, s[36:37]
	v_add_f32_e32 v104, v107, v235
	v_cndmask_b32_e64 v104, v249, v104, s[38:39]
	v_add_f32_e32 v196, v96, v232
	v_cndmask_b32_e64 v196, v249, v196, s[40:41]
	v_add_f32_e32 v195, v97, v233
	v_cndmask_b32_e64 v195, v249, v195, s[42:43]
	v_add_f32_e32 v97, v98, v234
	v_cndmask_b32_e64 v97, v249, v97, s[44:45]
	v_add_f32_e32 v96, v99, v235
	v_cndmask_b32_e64 v96, v249, v96, s[4:5]
	s_waitcnt lgkmcnt(4)
	v_add_f32_e32 v99, v92, v236
	v_cndmask_b32_e64 v99, v249, v99, s[30:31]
	v_add_f32_e32 v98, v93, v237
	v_cndmask_b32_e64 v98, v249, v98, s[34:35]
	v_add_f32_e32 v93, v94, v238
	v_cndmask_b32_e64 v93, v249, v93, s[36:37]
	v_add_f32_e32 v92, v95, v239
	v_cndmask_b32_e64 v92, v249, v92, s[38:39]
	v_add_f32_e32 v95, v88, v236
	v_cndmask_b32_e64 v95, v249, v95, s[40:41]
	v_add_f32_e32 v94, v89, v237
	v_cndmask_b32_e64 v94, v249, v94, s[42:43]
	v_add_f32_e32 v89, v90, v238
	v_cndmask_b32_e64 v89, v249, v89, s[44:45]
	v_add_f32_e32 v88, v91, v239
	v_cndmask_b32_e64 v88, v249, v88, s[4:5]
	s_waitcnt lgkmcnt(0)
	v_add_f32_e32 v91, v84, v240
	v_cndmask_b32_e64 v91, v249, v91, s[30:31]
	v_add_f32_e32 v90, v85, v241
	v_cndmask_b32_e64 v90, v249, v90, s[34:35]
	v_add_f32_e32 v198, v86, v242
	v_cndmask_b32_e64 v198, v249, v198, s[36:37]
	v_add_f32_e32 v197, v87, v243
	v_cndmask_b32_e64 v197, v249, v197, s[38:39]
	v_add_f32_e32 v202, v80, v240
	v_cndmask_b32_e64 v202, v249, v202, s[40:41]
	v_add_f32_e32 v199, v81, v241
	v_cndmask_b32_e64 v199, v249, v199, s[42:43]
	v_add_f32_e32 v81, v82, v242
	v_cndmask_b32_e64 v81, v249, v81, s[44:45]
	v_add_f32_e32 v80, v83, v243
	v_cndmask_b32_e64 v80, v249, v80, s[4:5]
	s_branch .LBB0_614
	s_nop 0
	s_nop 0
	s_nop 0
	s_nop 0
	s_nop 0
	s_nop 0
	s_nop 0
	s_nop 0
